# attn: key-tile rotation (2qb+7head)&31 instead of (2qb+5head)&31
# speedup vs baseline: 1.0556x; 1.0294x over previous
.Lp_top:
	s_lshl_b32 s6, s21, 20
	s_add_u32 s4, s4, s6
	s_addc_u32 s5, s5, 0
	v_lshlrev_b32_e32 v54, 4, v0
	v_mov_b32_e32 v55, v63
	s_lshl_b32 s3, s3, 1
	s_mul_i32 s20, s21, 7
	v_lshl_add_u64 v[4:5], s[4:5], 0, v[54:55]
	s_mov_b64 s[4:5], 0x1000000
	s_add_i32 s20, s20, s3
	v_lshl_add_u64 v[170:171], v[4:5], 0, s[4:5]
	s_and_b32 s22, s20, 31
	s_lshl_b32 s4, s20, 12
	s_lshl_b32 s12, s22, 13
	s_add_i32 s5, s4, 0x1000
	v_lshl_add_u64 v[58:59], v[170:171], 0, s[12:13]
	s_mov_b32 s3, 0x80000
	s_and_b32 s5, s5, 0x1f000
	v_add_co_u32_e32 v16, vcc, s3, v58
	s_lshl_b32 s12, s5, 1
	s_nop 0
	v_addc_co_u32_e32 v17, vcc, 0, v59, vcc
	v_lshl_add_u64 v[56:57], v[170:171], 0, s[12:13]
	global_load_dwordx4 v[4:7], v[58:59], off
	global_load_dwordx4 v[8:11], v[56:57], off
	global_load_dwordx4 v[12:15], v[16:17], off
	v_add_co_u32_e32 v16, vcc, s3, v56
	v_lshrrev_b32_e32 v184, 8, v0
	s_nop 0
	v_addc_co_u32_e32 v17, vcc, 0, v57, vcc
	global_load_dwordx4 v[16:19], v[16:17], off
	v_and_b32_e32 v20, 19, v0
	v_lshlrev_b32_e32 v21, 1, v0
	v_and_b32_e32 v2, 4, v2
	v_and_or_b32 v20, v21, 8, v20
	v_lshlrev_b32_e32 v101, 5, v184
	s_addk_i32 s4, 0x2000
	v_or3_b32 v2, v20, v2, v101
	s_and_b32 s4, s4, 0x1f000
	v_mul_u32_u24_e32 v2, 0x48, v2
	s_lshl_b32 s12, s4, 1
	v_lshlrev_b32_e32 v3, 3, v0
	v_lshlrev_b32_e32 v100, 1, v99
	v_lshlrev_b32_e32 v2, 1, v2
	v_lshl_add_u64 v[60:61], v[170:171], 0, s[12:13]
	v_and_b32_e32 v3, 56, v3
	v_add3_u32 v186, 0, v2, v100
	v_add_co_u32_e32 v2, vcc, s3, v60
	v_lshlrev_b32_e32 v68, 1, v3
	s_nop 0
	v_addc_co_u32_e32 v3, vcc, 0, v61, vcc
	global_load_dwordx4 v[162:165], v[60:61], off
	global_load_dwordx4 v[166:169], v[2:3], off
	v_lshrrev_b32_e32 v82, 3, v0
	v_mul_u32_u24_e32 v22, 0x48, v82
	v_lshlrev_b32_e32 v21, 1, v22
	v_add3_u32 v185, 0, v21, v68
	s_mov_b64 s[24:25], 0x80000
	s_add_i32 s17, s20, 3
	s_add_i32 s18, s20, 4
	v_mov_b32_e32 v62, v63
	v_lshrrev_b32_e32 v55, 6, v0
	v_mov_b32_e32 v83, 0
	v_mov_b32_e32 v84, 0
	v_lshl_add_u64 v[70:71], v[58:59], 0, s[24:25]
	v_lshl_add_u64 v[66:67], v[56:57], 0, s[24:25]
	v_lshl_add_u64 v[64:65], v[60:61], 0, s[24:25]
	s_waitcnt vmcnt(5)
	ds_write_b128 v185, v[4:7]
	s_waitcnt vmcnt(3)
	ds_write_b128 v185, v[12:15] offset:9216
	ds_write_b128 v185, v[8:11] offset:18432
	s_waitcnt vmcnt(2)
	ds_write_b128 v185, v[16:19] offset:27648
	s_waitcnt lgkmcnt(0)
	s_barrier
	ds_read_b128 v[2:5], v186
	ds_read_b128 v[38:41], v186 offset:32
	s_waitcnt lgkmcnt(1)
	v_mfma_f32_32x32x16_f16 v[2:17], v[2:5], v[114:117], 0
	ds_read_b128 v[18:21], v186 offset:9216
	ds_read_b128 v[46:49], v186 offset:9248
	s_waitcnt lgkmcnt(1)
	v_mfma_f32_32x32x16_f16 v[18:33], v[18:21], v[130:133], 0
	v_mfma_f32_32x32x16_f16 v[2:17], v[38:41], v[118:121], v[2:17]
	s_waitcnt lgkmcnt(0)
	v_mfma_f32_32x32x16_f16 v[18:33], v[46:49], v[134:137], v[18:33]
	ds_read_b128 v[38:41], v186 offset:64
	ds_read_b128 v[46:49], v186 offset:96
	s_waitcnt lgkmcnt(1)
	v_mfma_f32_32x32x16_f16 v[2:17], v[38:41], v[122:125], v[2:17]
	ds_read_b128 v[38:41], v186 offset:9280
	ds_read_b128 v[50:53], v186 offset:9312
	s_load_dwordx4 s[4:7], s[0:1], 0x38
	s_load_dwordx2 s[14:15], s[0:1], 0x8
	s_mov_b32 s0, -2
	s_mov_b32 s1, 0x3f800000
	s_waitcnt lgkmcnt(0)
	s_barrier
	v_mfma_f32_32x32x16_f16 v[18:33], v[38:41], v[138:141], v[18:33]
	v_mfma_f32_32x32x16_f16 v[2:17], v[46:49], v[126:129], v[2:17]
	v_mfma_f32_32x32x16_f16 v[18:33], v[50:53], v[142:145], v[18:33]
	s_lshl_b32 s12, s17, 13
	s_and_b32 s12, s12, 0x3e000
	s_add_u32 s28, s12, s3
	s_mov_b32 s29, 0
	v_lshl_add_u64 v[176:177], v[170:171], 0, s[12:13]
	global_load_dwordx4 v[50:53], v[176:177], off
	v_lshl_add_u64 v[176:177], v[170:171], 0, s[28:29]
	global_load_dwordx4 v[94:97], v[176:177], off
	s_nop 7
	s_cmp_eq_u32 s37, 1
	s_cbranch_scc0 .Lf_A
	v_mov_b32_e32 v83, 0xf149f2ca
	v_mov_b32_e32 v84, 0xf149f2ca
	s_branch .Ls_A

.Ll1_cont:
	ds_bpermute_b32 v2, v69, v84
	ds_bpermute_b32 v5, v69, v83
	v_max_f32_e32 v4, v84, v84
	v_max_f32_e32 v7, v83, v83
	ds_bpermute_b32 v3, v69, v63
	s_waitcnt lgkmcnt(2)
	v_max_f32_e32 v6, v2, v2
	v_max_f32_e32 v4, v4, v6
	v_sub_f32_e32 v6, v84, v4
	v_exp_f32_e32 v9, v6
	s_waitcnt lgkmcnt(1)
	v_max_f32_e32 v6, v5, v5
	v_sub_f32_e32 v2, v2, v4
	v_max_f32_e32 v6, v7, v6
	v_exp_f32_e32 v11, v2
	ds_bpermute_b32 v2, v69, v62
	v_sub_f32_e32 v5, v5, v6
	v_sub_f32_e32 v7, v83, v6
	v_exp_f32_e32 v10, v5
	v_exp_f32_e32 v8, v7
	v_cmp_gt_u32_e32 vcc, 32, v98
	s_waitcnt lgkmcnt(0)
	v_pk_mul_f32 v[2:3], v[10:11], v[2:3]
	s_nop 0
	v_pk_fma_f32 v[8:9], v[62:63], v[8:9], v[2:3]
	v_lshlrev_b32_e32 v2, 7, v184
	v_or3_b32 v10, v183, v2, v1
	s_and_saveexec_b64 s[0:1], vcc
	v_lshl_add_u32 v2, v10, 4, 0
	v_add_u32_e32 v2, 0x21000, v2
	v_mov_b32_e32 v5, v9
	v_mov_b32_e32 v7, v8
	ds_write_b128 v2, v[4:7]
	s_or_b64 exec, exec, s[0:1]
	s_lshl_b32 s12, s21, 7
	s_mov_b32 s3, 0
	v_or_b32_e32 v2, s12, v82
	s_lshl_b32 s13, s21, 11
	s_add_i32 s23, 0, 0x12000
	v_lshlrev_b32_e32 v2, 12, v2
	v_mov_b32_e32 v3, 0
	s_add_i32 s13, s13, s16
	s_lshl_b64 s[0:1], s[2:3], 13
	v_lshl_add_u64 v[12:13], s[14:15], 0, v[2:3]
	v_mov_b32_e32 v69, v3
	s_add_u32 s0, s10, s0
	v_lshl_add_u64 v[172:173], v[12:13], 0, v[68:69]
	s_addc_u32 s1, s11, s1
	s_lshl_b32 s10, s22, 7
	s_mov_b32 s11, s3
	s_waitcnt vmcnt(1)
	v_lshl_add_u64 v[36:37], v[172:173], 0, s[10:11]
	s_mov_b32 s10, 0x40000
	v_add_co_u32_e32 v38, vcc, s10, v36
	s_waitcnt lgkmcnt(0)
	s_barrier
	global_load_dwordx4 v[12:15], v[58:59], off
	global_load_dwordx4 v[16:19], v[70:71], off
	v_addc_co_u32_e32 v39, vcc, 0, v37, vcc
	global_load_dwordx4 v[20:23], v[56:57], off
	global_load_dwordx4 v[24:27], v[66:67], off
	global_load_dwordx4 v[28:31], v[36:37], off
	global_load_dwordx4 v[32:35], v[38:39], off
	v_add_f32_e32 v2, v78, v80
	s_movk_i32 s11, 0x1200
	v_add_f32_e32 v5, v79, v81
	s_mov_b32 s14, 0x3fb8aa3b
	v_lshlrev_b32_e32 v10, 4, v10
	v_mov_b32_e32 v36, s23
	v_mul_f32_e32 v37, 0x3fb8aa3b, v2
	v_mul_f32_e32 v38, 0x3fb8aa3b, v5
	v_xor_b32_e32 v10, 0x800, v10
	v_mad_u32_u24 v40, v55, s11, v36
	v_fma_f32 v36, v2, s14, -v37
	v_rndne_f32_e32 v39, v37
	v_fma_f32 v41, v5, s14, -v38
	s_waitcnt vmcnt(6)
	v_rndne_f32_e32 v42, v38
	v_add_u32_e32 v10, 0, v10
	v_fmac_f32_e32 v36, 0x32a5705f, v2
	v_sub_f32_e32 v37, v37, v39
	v_fmac_f32_e32 v41, 0x32a5705f, v5
	v_sub_f32_e32 v38, v38, v42
	v_add_u32_e32 v10, 0x21000, v10
	v_add_f32_e32 v44, v37, v36
	global_load_dwordx4 v[146:149], v[60:61], off
	global_load_dwordx4 v[150:153], v[64:65], off
	v_cvt_i32_f32_e32 v43, v39
	v_add_f32_e32 v41, v38, v41
	ds_read_b128 v[36:39], v10
	v_exp_f32_e32 v10, v44
	v_cvt_i32_f32_e32 v42, v42
	v_exp_f32_e32 v41, v41
	s_mov_b32 s21, 0xc2ce8ed0
	s_lshl_b32 s11, s20, 6
	s_add_i32 s14, s11, 64
	v_ldexp_f32 v10, v10, v43
	v_cmp_ngt_f32_e32 vcc, s21, v2
	s_mov_b32 s22, 0x42b17218
	s_and_b32 s14, s14, 0x7c0
	v_ldexp_f32 v41, v41, v42
	v_cndmask_b32_e32 v10, 0, v10, vcc
	v_cmp_ngt_f32_e32 vcc, s21, v5
	v_mov_b32_e32 v7, 0x7f800000
	v_max_f32_e32 v11, v4, v4
	s_mov_b32 s15, s3
	s_lshl_b32 s14, s14, 1
	s_waitcnt lgkmcnt(0)
	v_max_f32_e32 v42, v36, v36
	v_cndmask_b32_e32 v41, 0, v41, vcc
	v_cmp_nlt_f32_e32 vcc, s22, v2
	v_max_f32_e32 v187, v11, v42
	v_mov_b32_e32 v55, v3
	v_cndmask_b32_e32 v2, v7, v10, vcc
	v_cmp_nlt_f32_e32 vcc, s22, v5
	v_lshl_add_u64 v[10:11], v[172:173], 0, s[14:15]
	v_lshl_add_u64 v[178:179], s[0:1], 0, v[54:55]
	v_cndmask_b32_e32 v5, v7, v41, vcc
	v_sub_f32_e32 v2, v2, v5
	v_add_f32_e32 v41, 0x3e4ccccd, v2
	v_sub_f32_e32 v2, v4, v187
	v_max_f32_e32 v4, v6, v6
	s_and_b32 s1, s2, 7
	s_mulk_i32 s1, 0x380
	s_mulk_i32 s19, 0x1c0
	s_add_i32 s0, s20, 2
	s_waitcnt vmcnt(7)
	ds_write_b128 v185, v[12:15]
	s_waitcnt vmcnt(6)
	ds_write_b128 v185, v[16:19] offset:9216
	s_waitcnt vmcnt(5)
	ds_write_b128 v185, v[20:23] offset:18432
	s_waitcnt vmcnt(4)
	ds_write_b128 v185, v[24:27] offset:27648
	s_waitcnt vmcnt(3)
	ds_write_b128 v185, v[28:31] offset:36864
	s_waitcnt vmcnt(2)
	ds_write_b128 v185, v[32:35] offset:46080
	v_add_co_u32_e32 v12, vcc, s10, v10
	v_exp_f32_e32 v23, v2
	s_nop 0
	v_addc_co_u32_e32 v13, vcc, 0, v11, vcc
	global_load_dwordx4 v[154:157], v[10:11], off
	global_load_dwordx4 v[158:161], v[12:13], off
	s_waitcnt lgkmcnt(0)
	s_barrier
	ds_read_b128 v[10:13], v186
	v_sub_f32_e32 v2, v36, v187
	v_exp_f32_e32 v25, v2
	v_max_f32_e32 v2, v38, v38
	v_max_f32_e32 v188, v4, v2
	v_sub_f32_e32 v2, v6, v188
	v_exp_f32_e32 v22, v2
	v_sub_f32_e32 v2, v38, v188
	v_exp_f32_e32 v24, v2
	ds_read_b128 v[14:17], v186 offset:9216
	ds_read_b128 v[18:21], v186 offset:32
	s_waitcnt lgkmcnt(2)
	v_mfma_f32_32x32x16_f16 v[66:81], v[10:13], v[114:117], 0
	v_mov_b32_e32 v36, v39
	v_mul_f32_e64 v10, v36, v24
	v_mul_f32_e64 v11, v37, v25
	ds_read_b128 v[4:7], v186 offset:9248
	s_add_i32 s1, s1, s19
	s_mov_b32 s14, 0x30000
	s_mov_b32 s15, 0x80000
	s_mov_b32 s19, 0
	s_waitcnt lgkmcnt(2)
	v_mfma_f32_32x32x16_f16 v[82:97], v[14:17], v[130:133], 0
	v_fma_f32 v16, v8, v22, v10
	v_fma_f32 v17, v9, v23, v11
	v_log_f32_e32 v238, v17
	s_nop 0
	v_add_f32_e32 v187, v187, v238
	v_sub_f32_e32 v240, 0, v187
	v_sub_f32_e32 v241, 0, v187
	v_sub_f32_e32 v242, 0, v187
	v_sub_f32_e32 v243, 0, v187
	v_sub_f32_e32 v244, 0, v187
	v_sub_f32_e32 v245, 0, v187
	v_sub_f32_e32 v246, 0, v187
	v_sub_f32_e32 v247, 0, v187
	v_sub_f32_e32 v248, 0, v187
	v_sub_f32_e32 v249, 0, v187
	v_sub_f32_e32 v250, 0, v187
	v_sub_f32_e32 v251, 0, v187
	v_sub_f32_e32 v252, 0, v187
	v_sub_f32_e32 v253, 0, v187
	v_sub_f32_e32 v254, 0, v187
	v_sub_f32_e32 v255, 0, v187
	v_lshrrev_b32_e32 v22, 3, v98
	v_or3_b32 v2, s13, v183, v22
	v_lshlrev_b64 v[8:9], 13, v[2:3]
	v_lshl_add_u64 v[8:9], s[4:5], 0, v[8:9]
	v_lshlrev_b32_e32 v2, 2, v101
	v_lshl_add_u64 v[8:9], v[8:9], 0, v[2:3]
	v_and_b32_e32 v2, 0x70, v54
	v_lshl_add_u64 v[174:175], v[8:9], 0, v[2:3]
	ds_read_b128 v[8:11], v186 offset:64
	s_waitcnt lgkmcnt(2)
	v_mfma_f32_32x32x16_f16 v[66:81], v[18:21], v[118:121], v[66:81]
	v_div_scale_f32 v18, s[4:5], v16, v16, -v41
	v_rcp_f32_e32 v19, v18
	v_div_scale_f32 v20, vcc, -v41, v16, -v41
	s_mov_b32 s13, 0x20000
	v_mov_b32_e32 v24, v3
	s_waitcnt lgkmcnt(1)
	v_mfma_f32_32x32x16_f16 v[82:97], v[4:7], v[134:137], v[82:97]
	v_fma_f32 v4, -v18, v19, 1.0
	v_fmac_f32_e32 v19, v4, v19
	v_mul_f32_e32 v21, v20, v19
	ds_read_b128 v[4:7], v186 offset:9280
	ds_read_b128 v[12:15], v186 offset:96
	v_mov_b32_e32 v25, v3
	v_mov_b32_e32 v26, v3
	v_mov_b32_e32 v27, v3
	s_waitcnt lgkmcnt(2)
	v_mfma_f32_32x32x16_f16 v[66:81], v[8:11], v[122:125], v[66:81]
	v_fma_f32 v8, -v18, v21, v20
	v_fmac_f32_e32 v21, v8, v19
	v_fma_f32 v18, -v18, v21, v20
	v_div_scale_f32 v20, s[4:5], v17, v17, 1.0
	v_rcp_f32_e32 v23, v20
	ds_read_b128 v[8:11], v186 offset:9312
	s_waitcnt lgkmcnt(2)
	v_mfma_f32_32x32x16_f16 v[82:97], v[4:7], v[138:141], v[82:97]
	v_div_fmas_f32 v4, v18, v19, v21
	v_div_fixup_f32 v176, v4, v16, -v41
	v_fma_f32 v4, -v20, v23, 1.0
	v_fmac_f32_e32 v23, v4, v23
	v_div_scale_f32 v4, vcc, 1.0, v17, 1.0
	v_mul_f32_e32 v5, v4, v23
	v_fma_f32 v6, -v20, v5, v4
	v_fmac_f32_e32 v5, v6, v23
	s_waitcnt lgkmcnt(1)
	v_mfma_f32_32x32x16_f16 v[66:81], v[12:15], v[126:129], v[66:81]
	v_fma_f32 v4, -v20, v5, v4
	v_div_fmas_f32 v4, v4, v23, v5
	v_div_fixup_f32 v177, v4, v17, 1.0
	v_mul_u32_u24_e32 v4, 0x90, v22
	v_add3_u32 v189, v40, v4, v2
	v_mul_u32_u24_e32 v2, 0x90, v1
	v_lshlrev_b32_e32 v4, 2, v99
	s_waitcnt lgkmcnt(0)
	v_mfma_f32_32x32x16_f16 v[82:97], v[8:11], v[142:145], v[82:97]
	v_add3_u32 v190, v40, v2, v4
	v_mul_u32_u24_e32 v2, 0x48, v1
	v_lshl_add_u32 v2, v2, 1, 0
	v_lshlrev_b32_e32 v4, 1, v101
	v_add3_u32 v191, v2, v4, v100
	s_mov_b32 s4, 0x3f800000
	s_mov_b32 s5, 0x10000
	v_mov_b32_e32 v2, v3
	v_mov_b32_e32 v4, v3
	v_mov_b32_e32 v5, v3
	v_mov_b32_e32 v6, v3
	v_mov_b32_e32 v7, v3
	v_mov_b32_e32 v8, v3
	v_mov_b32_e32 v9, v3
	v_mov_b32_e32 v10, v3
	v_mov_b32_e32 v11, v3
	v_mov_b32_e32 v12, v3
	v_mov_b32_e32 v13, v3
	v_mov_b32_e32 v14, v3
	v_mov_b32_e32 v15, v3
	v_mov_b32_e32 v16, v3
	v_mov_b32_e32 v17, v3
	v_mov_b32_e32 v18, v3
	v_mov_b32_e32 v19, v3
	v_mov_b32_e32 v20, v3
	v_mov_b32_e32 v21, v3
	v_mov_b32_e32 v22, v3
	v_mov_b32_e32 v23, v3
	v_mov_b32_e32 v28, v3
	v_mov_b32_e32 v29, v3
	v_mov_b32_e32 v30, v3
	v_mov_b32_e32 v31, v3
	v_mov_b32_e32 v32, v3
	v_mov_b32_e32 v33, v3
	v_mov_b32_e32 v34, v3
	v_mov_b32_e32 v35, v3
	v_mov_b32_e32 v36, v3
	v_mov_b32_e32 v37, v3
	v_mov_b32_e32 v38, v3
	v_mov_b32_e32 v39, v3
	v_mov_b32_e32 v40, v3
	v_mov_b32_e32 v41, v3
	v_mov_b32_e32 v42, v3
	v_mov_b32_e32 v43, v3
	v_mov_b32_e32 v44, v3
	v_mov_b32_e32 v45, v3
	v_mov_b32_e32 v46, v3
	v_mov_b32_e32 v47, v3
	v_mov_b32_e32 v48, v3
	v_mov_b32_e32 v49, v3
	v_mov_b32_e32 v50, v3
	v_mov_b32_e32 v51, v3
	v_mov_b32_e32 v52, v3
	v_mov_b32_e32 v53, v3
	v_mov_b32_e32 v54, v3
	v_mov_b32_e32 v56, v3
	v_mov_b32_e32 v57, v3
	v_mov_b32_e32 v58, v3
	v_mov_b32_e32 v59, v3
	v_mov_b32_e32 v60, v3
	v_mov_b32_e32 v61, v3
	v_mov_b32_e32 v62, v3
	v_mov_b32_e32 v63, v3
	v_mov_b32_e32 v64, v3
	v_mov_b32_e32 v65, v3
	v_add_u32_e32 v192, 0xd800, v191
	v_sub_f32_e32 v66, v66, v187
	v_sub_f32_e32 v67, v67, v187
	v_sub_f32_e32 v68, v68, v187
	v_sub_f32_e32 v69, v69, v187
	v_sub_f32_e32 v70, v70, v187
	v_sub_f32_e32 v71, v71, v187
	v_sub_f32_e32 v72, v72, v187
	v_sub_f32_e32 v73, v73, v187
	v_sub_f32_e32 v74, v74, v187
	v_sub_f32_e32 v75, v75, v187
	v_sub_f32_e32 v76, v76, v187
	v_sub_f32_e32 v77, v77, v187
	v_sub_f32_e32 v78, v78, v187
	v_sub_f32_e32 v79, v79, v187
	v_sub_f32_e32 v80, v80, v187
	v_sub_f32_e32 v81, v81, v187
	s_mov_b32 s27, 0x42c80000
	v_cmp_gt_f32_e64 vcc, |v188|, s27
	s_cbranch_vccnz .Ll2_gen
	v_sub_f32_e32 v238, 0, v188
	v_exp_f32_e32 v238, v238
	s_nop 0
	v_mul_f32_e32 v176, v176, v238
	s_barrier
	s_branch .Ll2f_top
